# indexer head loop rescheduled: each chain's fmas issued two MFMAs after the chain's last MFMA, hazard s_nops removed (85 -> 17 wait states per body)
# baseline (speedup 1.0000x reference)
; #define LAS __attribute__((address_space(3)))
; #define IDX_ACC(cc, jj) do { float s0 = fmaf(wh, __builtin_fabsf(cc[0]), sacc[jj][0]); sacc[jj][0] = s0; \
;                             _Pragma("unroll") for (int r = 1; r < 16; ++r) { float a_ = sacc[jj][r]; asm("v_fma_f32 %0, %1, |%2|, %0" : "+v"(a_) : "v"(wh), "v"(cc[r]), "v"(s0)); sacc[jj][r] = a_; } } while (0)
; __global__ void __launch_bounds__(NTHREADS, 2) mega_fwd(Args args) {
;     ...
;                 for (int h = 0; h < NIH; ++h) {
;                     bf16x8 qf[4];
; #pragma unroll
;                     for (int ks = 0; ks < 4; ++ks) qf[ks] = *(const LAS bf16x8*)(Qs + (((h * 4 + ks) * 2 + hi5) * 32 + r32) * 16);
;                     const float wh = Ws[h * 32 + r32];
; #pragma unroll
;                     for (int jp = 0; jp < 4; jp += 2) { f32x16 c0 = f32x16{}, c1 = f32x16{};
; #pragma unroll
;                         for (int ks = 0; ks < 4; ++ks) { c0 = __builtin_amdgcn_mfma_f32_32x32x16_bf16(kf[jp][ks], qf[ks], c0, 0, 0, 0); c1 = __builtin_amdgcn_mfma_f32_32x32x16_bf16(kf[jp + 1][ks], qf[ks], c1, 0, 0, 0); }
;                         __builtin_amdgcn_sched_barrier(0);
;     ...
;                         IDX_ACC(c0, jp); IDX_ACC(c1, jp + 1);
.LBB0_656:
	v_add_u32_e32 v58, s7, v233
	ds_read_b128 v[42:45], v58
	ds_read_b128 v[46:49], v58 offset:1024
	ds_read_b128 v[50:53], v58 offset:2048
	ds_read_b128 v[54:57], v58 offset:3072
	s_nop 4
	v_add_u32_e32 v2, 0xffffff80, v234
	ds_read_b32 v235, v2
	s_waitcnt lgkmcnt(4)
	v_mfma_f32_32x32x16_bf16 v[10:25], v[66:69], v[42:45], 0
	s_waitcnt lgkmcnt(3)
	v_mfma_f32_32x32x16_bf16 v[10:25], v[70:73], v[46:49], v[10:25]
	s_waitcnt lgkmcnt(2)
	v_mfma_f32_32x32x16_bf16 v[10:25], v[74:77], v[50:53], v[10:25]
	s_waitcnt lgkmcnt(1)
	v_mfma_f32_32x32x16_bf16 v[10:25], v[78:81], v[54:57], v[10:25]
	v_mfma_f32_32x32x16_bf16 v[26:41], v[82:85], v[42:45], 0
	v_mfma_f32_32x32x16_bf16 v[26:41], v[86:89], v[46:49], v[26:41]
	s_waitcnt lgkmcnt(0)
	v_fma_f32 v206, v235, |v10|, v206
	v_fma_f32 v207, v235, |v11|, v207
	v_fma_f32 v208, v235, |v12|, v208
	v_fma_f32 v209, v235, |v13|, v209
	v_fma_f32 v210, v235, |v14|, v210
	v_fma_f32 v211, v235, |v15|, v211
	v_fma_f32 v212, v235, |v16|, v212
	v_fma_f32 v213, v235, |v17|, v213
	v_fma_f32 v214, v235, |v18|, v214
	v_fma_f32 v215, v235, |v19|, v215
	v_fma_f32 v216, v235, |v20|, v216
	v_fma_f32 v217, v235, |v21|, v217
	v_fma_f32 v218, v235, |v22|, v218
	v_fma_f32 v219, v235, |v23|, v219
	v_mfma_f32_32x32x16_bf16 v[4:19], v[98:101], v[42:45], 0
	v_fma_f32 v220, v235, |v24|, v220
	v_fma_f32 v221, v235, |v25|, v221
	v_mfma_f32_32x32x16_bf16 v[26:41], v[90:93], v[50:53], v[26:41]
	v_mfma_f32_32x32x16_bf16 v[4:19], v[102:105], v[46:49], v[4:19]
	v_mfma_f32_32x32x16_bf16 v[26:41], v[94:97], v[54:57], v[26:41]
	v_mfma_f32_32x32x16_bf16 v[4:19], v[106:109], v[50:53], v[4:19]
	v_mfma_f32_32x32x16_bf16 v[4:19], v[114:117], v[54:57], v[4:19]
	v_fma_f32 v190, v235, |v26|, v190
	v_fma_f32 v191, v235, |v27|, v191
	v_fma_f32 v192, v235, |v28|, v192
	v_fma_f32 v193, v235, |v29|, v193
	v_fma_f32 v194, v235, |v30|, v194
	v_fma_f32 v195, v235, |v31|, v195
	v_fma_f32 v196, v235, |v32|, v196
	v_fma_f32 v197, v235, |v33|, v197
	v_fma_f32 v198, v235, |v34|, v198
	v_fma_f32 v199, v235, |v35|, v199
	v_fma_f32 v200, v235, |v36|, v200
	v_fma_f32 v201, v235, |v37|, v201
	v_fma_f32 v202, v235, |v38|, v202
	v_fma_f32 v203, v235, |v39|, v203
	v_fma_f32 v204, v235, |v40|, v204
	v_fma_f32 v205, v235, |v41|, v205
	v_mfma_f32_32x32x16_bf16 v[20:35], v[130:133], v[42:45], 0
	v_fma_f32 v188, v235, |v4|, v188
	v_fma_f32 v189, v235, |v5|, v189
	v_fma_f32 v186, v235, |v6|, v186
	v_fma_f32 v187, v235, |v7|, v187
	v_fma_f32 v184, v235, |v8|, v184
	v_fma_f32 v185, v235, |v9|, v185
	v_fma_f32 v182, v235, |v10|, v182
	v_mfma_f32_32x32x16_bf16 v[20:35], v[134:137], v[46:49], v[20:35]
	v_fma_f32 v183, v235, |v11|, v183
	v_fma_f32 v180, v235, |v12|, v180
	v_fma_f32 v181, v235, |v13|, v181
	v_fma_f32 v178, v235, |v14|, v178
	v_fma_f32 v179, v235, |v15|, v179
	v_fma_f32 v176, v235, |v16|, v176
	v_fma_f32 v177, v235, |v17|, v177
	v_mfma_f32_32x32x16_bf16 v[20:35], v[138:141], v[50:53], v[20:35]
	ds_read_b128 v[50:53], v58 offset:4096
	ds_read_b128 v[62:65], v58 offset:6144
	v_fma_f32 v174, v235, |v18|, v174
	v_fma_f32 v175, v235, |v19|, v175
	v_mfma_f32_32x32x16_bf16 v[20:35], v[142:145], v[54:57], v[20:35]
	ds_read_b128 v[54:57], v58 offset:5120
	ds_read_b128 v[58:61], v58 offset:7168
	s_waitcnt lgkmcnt(3)
	v_mfma_f32_32x32x16_bf16 v[2:17], v[66:69], v[50:53], 0
	s_waitcnt lgkmcnt(1)
	v_mfma_f32_32x32x16_bf16 v[2:17], v[70:73], v[54:57], v[2:17]
	v_fma_f32 v172, v235, |v20|, v172
	v_fma_f32 v173, v235, |v21|, v173
	v_fma_f32 v170, v235, |v22|, v170
	v_fma_f32 v171, v235, |v23|, v171
	v_fma_f32 v168, v235, |v24|, v168
	v_fma_f32 v169, v235, |v25|, v169
	v_fma_f32 v166, v235, |v26|, v166
	v_fma_f32 v167, v235, |v27|, v167
	v_fma_f32 v164, v235, |v28|, v164
	v_fma_f32 v165, v235, |v29|, v165
	v_fma_f32 v162, v235, |v30|, v162
	v_fma_f32 v163, v235, |v31|, v163
	v_fma_f32 v160, v235, |v32|, v160
	v_fma_f32 v161, v235, |v33|, v161
	v_mfma_f32_32x32x16_bf16 v[2:17], v[74:77], v[62:65], v[2:17]
	v_fma_f32 v158, v235, |v34|, v158
	v_fma_f32 v159, v235, |v35|, v159
	ds_read_b32 v235, v234
	s_waitcnt lgkmcnt(1)
	v_mfma_f32_32x32x16_bf16 v[2:17], v[78:81], v[58:61], v[2:17]
	v_mfma_f32_32x32x16_bf16 v[34:49], v[82:85], v[50:53], 0
	v_mfma_f32_32x32x16_bf16 v[34:49], v[86:89], v[54:57], v[34:49]
	s_waitcnt lgkmcnt(0)
; #define LAS __attribute__((address_space(3)))
; #define IDX_ACC(cc, jj) do { float s0 = fmaf(wh, __builtin_fabsf(cc[0]), sacc[jj][0]); sacc[jj][0] = s0; \
;                             _Pragma("unroll") for (int r = 1; r < 16; ++r) { float a_ = sacc[jj][r]; asm("v_fma_f32 %0, %1, |%2|, %0" : "+v"(a_) : "v"(wh), "v"(cc[r]), "v"(s0)); sacc[jj][r] = a_; } } while (0)
; __global__ void __launch_bounds__(NTHREADS, 2) mega_fwd(Args args) {
;     ...
;                 for (int h = 0; h < NIH; ++h) {
;                     bf16x8 qf[4];
; #pragma unroll
;                     for (int ks = 0; ks < 4; ++ks) qf[ks] = *(const LAS bf16x8*)(Qs + (((h * 4 + ks) * 2 + hi5) * 32 + r32) * 16);
;                     const float wh = Ws[h * 32 + r32];
; #pragma unroll
;                     for (int jp = 0; jp < 4; jp += 2) { f32x16 c0 = f32x16{}, c1 = f32x16{};
; #pragma unroll
;                         for (int ks = 0; ks < 4; ++ks) { c0 = __builtin_amdgcn_mfma_f32_32x32x16_bf16(kf[jp][ks], qf[ks], c0, 0, 0, 0); c1 = __builtin_amdgcn_mfma_f32_32x32x16_bf16(kf[jp + 1][ks], qf[ks], c1, 0, 0, 0); }
;                         __builtin_amdgcn_sched_barrier(0);
;     ...
;                         IDX_ACC(c0, jp); IDX_ACC(c1, jp + 1);
;     ...
;                     }
;                 }
	v_fma_f32 v206, v235, |v2|, v206
	v_fma_f32 v207, v235, |v3|, v207
	v_fma_f32 v208, v235, |v4|, v208
	v_fma_f32 v209, v235, |v5|, v209
	v_fma_f32 v210, v235, |v6|, v210
	v_fma_f32 v211, v235, |v7|, v211
	v_fma_f32 v212, v235, |v8|, v212
	v_fma_f32 v213, v235, |v9|, v213
	v_fma_f32 v214, v235, |v10|, v214
	v_fma_f32 v215, v235, |v11|, v215
	v_fma_f32 v216, v235, |v12|, v216
	v_fma_f32 v217, v235, |v13|, v217
	v_fma_f32 v218, v235, |v14|, v218
	v_fma_f32 v219, v235, |v15|, v219
	v_mfma_f32_32x32x16_bf16 v[18:33], v[98:101], v[50:53], 0
	v_fma_f32 v220, v235, |v16|, v220
	v_fma_f32 v221, v235, |v17|, v221
	v_mfma_f32_32x32x16_bf16 v[34:49], v[90:93], v[62:65], v[34:49]
	v_mfma_f32_32x32x16_bf16 v[18:33], v[102:105], v[54:57], v[18:33]
	v_mfma_f32_32x32x16_bf16 v[34:49], v[94:97], v[58:61], v[34:49]
	v_mfma_f32_32x32x16_bf16 v[18:33], v[106:109], v[62:65], v[18:33]
	v_mfma_f32_32x32x16_bf16 v[18:33], v[114:117], v[58:61], v[18:33]
	v_fma_f32 v190, v235, |v34|, v190
	v_fma_f32 v191, v235, |v35|, v191
	v_fma_f32 v192, v235, |v36|, v192
	v_fma_f32 v193, v235, |v37|, v193
	v_fma_f32 v194, v235, |v38|, v194
	v_fma_f32 v195, v235, |v39|, v195
	v_fma_f32 v196, v235, |v40|, v196
	v_fma_f32 v197, v235, |v41|, v197
	v_fma_f32 v198, v235, |v42|, v198
	v_fma_f32 v199, v235, |v43|, v199
	v_fma_f32 v200, v235, |v44|, v200
	v_fma_f32 v201, v235, |v45|, v201
	v_fma_f32 v202, v235, |v46|, v202
	v_fma_f32 v203, v235, |v47|, v203
	v_fma_f32 v204, v235, |v48|, v204
	v_fma_f32 v205, v235, |v49|, v205
	v_mfma_f32_32x32x16_bf16 v[2:17], v[130:133], v[50:53], 0
	s_addk_i32 s7, 0x2000
	v_fma_f32 v188, v235, |v18|, v188
	v_fma_f32 v189, v235, |v19|, v189
	v_fma_f32 v186, v235, |v20|, v186
	v_fma_f32 v187, v235, |v21|, v187
	v_fma_f32 v184, v235, |v22|, v184
	v_fma_f32 v185, v235, |v23|, v185
	v_fma_f32 v182, v235, |v24|, v182
	v_mfma_f32_32x32x16_bf16 v[2:17], v[134:137], v[54:57], v[2:17]
	s_cmp_lg_u32 s7, 0x10000
	v_add_u32_e32 v234, 0x100, v234
	v_fma_f32 v183, v235, |v25|, v183
	v_fma_f32 v180, v235, |v26|, v180
	v_fma_f32 v181, v235, |v27|, v181
	v_fma_f32 v178, v235, |v28|, v178
	v_fma_f32 v179, v235, |v29|, v179
	v_fma_f32 v176, v235, |v30|, v176
	v_fma_f32 v177, v235, |v31|, v177
	v_mfma_f32_32x32x16_bf16 v[2:17], v[138:141], v[62:65], v[2:17]
	v_fma_f32 v174, v235, |v32|, v174
	v_fma_f32 v175, v235, |v33|, v175
	v_mfma_f32_32x32x16_bf16 v[2:17], v[142:145], v[58:61], v[2:17]
	s_nop 11
	v_fma_f32 v172, v235, |v2|, v172
	v_fma_f32 v173, v235, |v3|, v173
	v_fma_f32 v170, v235, |v4|, v170
	v_fma_f32 v171, v235, |v5|, v171
	v_fma_f32 v168, v235, |v6|, v168
	v_fma_f32 v169, v235, |v7|, v169
	v_fma_f32 v166, v235, |v8|, v166
	v_fma_f32 v167, v235, |v9|, v167
	v_fma_f32 v164, v235, |v10|, v164
	v_fma_f32 v165, v235, |v11|, v165
	v_fma_f32 v162, v235, |v12|, v162
	v_fma_f32 v163, v235, |v13|, v163
	v_fma_f32 v160, v235, |v14|, v160
	v_fma_f32 v161, v235, |v15|, v161
	v_fma_f32 v158, v235, |v16|, v158
	v_fma_f32 v159, v235, |v17|, v159
	s_cbranch_scc1 .LBB0_656
; __global__ void __launch_bounds__(NTHREADS, 2) mega_fwd(Args args) {
;     ...
;             if (act) {
; #pragma unroll
;                 for (int j = 0; j < 4; ++j)
; #pragma unroll
;                     for (int ks = 0; ks < 4; ++ks) kf[j][ks] = *(const bf16x8*)(KI + (size_t)(kb0 + 32 * j + r32) * IDD + ks * 16 + hi5 * 8);
; #pragma unroll
;                 for (int ks = 0; ks < 4; ++ks) qlf[ks] = *(const bf16x8*)(QLIN + (size_t)(q0 + r32) * IDD + ks * 16 + hi5 * 8);
;     ...
;                 for (int j = 0; j < 4; ++j) { f32x16 c = f32x16{};
; #pragma unroll
;                     for (int ks = 0; ks < 4; ++ks) c = __builtin_amdgcn_mfma_f32_32x32x16_bf16(kf[j][ks], qlf[ks], c, 0, 0, 0);
; #pragma unroll
;                     for (int r = 0; r < 16; ++r) sacc[j][r] = 0.5f * (sacc[j][r] + c[r]); }
;                 float* srow = SCORES + (size_t)(q0 + r32) * S;
; #pragma unroll
;                 for (int j = 0; j < 4; ++j) if (kb0 + 32 * j < nadm) {
; #pragma unroll
;                     for (int rg = 0; rg < 4; ++rg) *(f32x4*)(srow + kb0 + 32 * j + 8 * rg + 4 * hi5) = (f32x4){sacc[j][4 * rg], sacc[j][4 * rg + 1], sacc[j][4 * rg + 2], sacc[j][4 * rg + 3]}; }
;             }
;             if (has_next) { Wsb[(buf ^ 1) * 512 + (tid >> 5) * 32 + (tid & 31)] = wn; q0 = nq0; seg = nseg2; nadm = nnadm; buf ^= 1; }
	s_xor_b32 s7, s25, 1
	v_lshl_add_u32 v2, s7, 11, v229
	s_waitcnt vmcnt(0)
	ds_write_b32 v2, v232
	v_mfma_f32_32x32x16_bf16 v[50:65], v[66:69], v[110:113], 0
	v_lshlrev_b64 v[2:3], 15, v[156:157]
	v_lshl_add_u64 v[2:3], s[2:3], 0, v[2:3]
	s_ashr_i32 s7, s6, 31
	v_lshl_add_u64 v[2:3], s[6:7], 2, v[2:3]
	v_lshl_add_u64 v[156:157], v[2:3], 0, v[148:149]
	s_or_b32 s7, s6, 32
	s_cmp_ge_i32 s7, s28
	v_mfma_f32_32x32x16_bf16 v[34:49], v[82:85], v[110:113], 0
	v_mfma_f32_32x32x16_bf16 v[18:33], v[98:101], v[110:113], 0
	v_mfma_f32_32x32x16_bf16 v[2:17], v[130:133], v[110:113], 0
	v_mfma_f32_32x32x16_bf16 v[50:65], v[70:73], v[118:121], v[50:65]
	v_mfma_f32_32x32x16_bf16 v[34:49], v[86:89], v[118:121], v[34:49]
	v_mfma_f32_32x32x16_bf16 v[18:33], v[102:105], v[118:121], v[18:33]
	v_mfma_f32_32x32x16_bf16 v[2:17], v[134:137], v[118:121], v[2:17]
	v_mfma_f32_32x32x16_bf16 v[50:65], v[74:77], v[122:125], v[50:65]
	v_mfma_f32_32x32x16_bf16 v[34:49], v[90:93], v[122:125], v[34:49]
	v_mfma_f32_32x32x16_bf16 v[18:33], v[106:109], v[122:125], v[18:33]
	v_mfma_f32_32x32x16_bf16 v[2:17], v[138:141], v[122:125], v[2:17]
	v_mfma_f32_32x32x16_bf16 v[50:65], v[78:81], v[126:129], v[50:65]
	v_mfma_f32_32x32x16_bf16 v[34:49], v[94:97], v[126:129], v[34:49]
	s_nop 10
	v_add_f32_e64 v52, v52, v208
	v_add_f32_e64 v53, v53, v209
	v_add_f32_e64 v50, v50, v206
	v_add_f32_e64 v51, v51, v207
	v_add_f32_e64 v56, v56, v212
	v_add_f32_e64 v57, v57, v213
	v_pk_add_f32 v[54:55], v[54:55], v[210:211]
	v_pk_mul_f32 v[52:53], v[52:53], 0.5 op_sel_hi:[1,0]
	v_pk_mul_f32 v[50:51], v[50:51], 0.5 op_sel_hi:[1,0]
	v_pk_add_f32 v[60:61], v[60:61], v[216:217]
	v_mfma_f32_32x32x16_bf16 v[18:33], v[114:117], v[126:129], v[18:33]
	v_add_f32_e64 v58, v58, v214
	v_add_f32_e64 v59, v59, v215
	global_store_dwordx4 v[156:157], v[50:53], off
	v_add_f32_e64 v64, v64, v220
	v_add_f32_e64 v65, v65, v221
	v_pk_add_f32 v[62:63], v[62:63], v[218:219]
	v_pk_mul_f32 v[52:53], v[56:57], 0.5 op_sel_hi:[1,0]
	v_pk_mul_f32 v[50:51], v[54:55], 0.5 op_sel_hi:[1,0]
	global_store_dwordx4 v[156:157], v[50:53], off offset:32
	v_mfma_f32_32x32x16_bf16 v[2:17], v[142:145], v[126:129], v[2:17]
	s_cmp_eq_u64 s[10:11], 0
	s_cbranch_scc1 .Lidx_nla_skip
	s_lshl_b32 s7, s13, 10
	s_add_i32 s7, s7, s26
	s_cmp_ge_i32 s7, s30
	s_cbranch_scc1 .Lidx_nla_skip
	v_or_b32_e32 v236, s7, v1
	v_ashrrev_i32_e32 v237, 31, v236
	v_lshlrev_b64 v[238:239], 7, v[236:237]
	v_lshl_add_u64 v[238:239], v[150:151], 0, v[238:239]
	global_load_dwordx4 v[66:69], v[238:239], off
	global_load_dwordx4 v[70:73], v[238:239], off offset:32
	global_load_dwordx4 v[74:77], v[238:239], off offset:64
	global_load_dwordx4 v[78:81], v[238:239], off offset:96
	v_or_b32_e32 v238, 32, v236
	v_ashrrev_i32_e32 v239, 31, v238
	v_lshlrev_b64 v[238:239], 7, v[238:239]
	v_lshl_add_u64 v[238:239], v[150:151], 0, v[238:239]
	global_load_dwordx4 v[82:85], v[238:239], off
	global_load_dwordx4 v[86:89], v[238:239], off offset:32
	global_load_dwordx4 v[90:93], v[238:239], off offset:64
	global_load_dwordx4 v[94:97], v[238:239], off offset:96
	v_or_b32_e32 v238, 64, v236
	v_ashrrev_i32_e32 v239, 31, v238
	v_lshlrev_b64 v[238:239], 7, v[238:239]
	v_lshl_add_u64 v[238:239], v[150:151], 0, v[238:239]
	global_load_dwordx4 v[98:101], v[238:239], off
	global_load_dwordx4 v[102:105], v[238:239], off offset:32
	global_load_dwordx4 v[106:109], v[238:239], off offset:64
	global_load_dwordx4 v[114:117], v[238:239], off offset:96
	v_or_b32_e32 v238, 96, v236
	v_ashrrev_i32_e32 v239, 31, v238
	v_lshlrev_b64 v[238:239], 7, v[238:239]
	v_lshl_add_u64 v[238:239], v[150:151], 0, v[238:239]
	global_load_dwordx4 v[130:133], v[238:239], off
	global_load_dwordx4 v[134:137], v[238:239], off offset:32
	global_load_dwordx4 v[138:141], v[238:239], off offset:64
	global_load_dwordx4 v[142:145], v[238:239], off offset:96
	v_add_u32_e32 v238, s12, v1
	v_ashrrev_i32_e32 v239, 31, v238
	v_lshlrev_b64 v[238:239], 7, v[238:239]
	v_lshl_add_u64 v[238:239], v[152:153], 0, v[238:239]
	global_load_dwordx4 v[110:113], v[238:239], off
	global_load_dwordx4 v[118:121], v[238:239], off offset:32
	global_load_dwordx4 v[122:125], v[238:239], off offset:64
	global_load_dwordx4 v[126:129], v[238:239], off offset:96
	s_mov_b32 s98, 1
